# v16 + nt hint on the scan phase's YB loads (read once, long evicted from MALL)
# speedup vs baseline: 1.0001x; 1.0001x over previous
; DI bf16_t f2bf(float f) { return (bf16_t)(pk_bf16(f, 0.f) & 0xffffu); }
; DI float bf2f(unsigned b) { return __uint_as_float(b << 16); }
; DI float bflo(unsigned p) { return __uint_as_float(p << 16); }
; DI float bfhi(unsigned p) { return __uint_as_float(p & 0xffff0000u); }
; DI void phase_scan2(const Ctx& c) {
;     ...
;     for (int item = c.blk; item < 256; item += c.G) {
;         const int bc = item >> 1, b = bc >> 6, chunk = bc & 63, ch = (item & 1) * 512 + c.tid;
;         float h = 0.f;
;         {
;             unsigned w[NMETA]; float y[NMETA];
; #pragma unroll
;             for (int m = 0; m < NMETA; ++m) { const size_t row = (size_t)MR + b * NMETA + m; w[m] = AB[row * 1024 + ch]; y[m] = bf2f(YB[row * 1024 + ch]); }
; #pragma unroll
;             for (int m = 0; m < NMETA; ++m) { const size_t row = (size_t)MR + b * NMETA + m; h = __expf(bflo(w[m])) * h + bfhi(w[m]); if (chunk == 0) Z[row * 1024 + ch] = f2bf(y[m] * h); }
;         }
; #pragma unroll 1
.LBB0_739:
	s_lshl_b32 s0, s54, 9
	s_ashr_i32 s60, s54, 7
	s_and_b32 s0, s0, 0x200
	v_add_u32_e32 v8, s0, v0
	s_lshl_b32 s0, s60, 4
	s_add_i32 s2, s0, 0x8000
	s_ashr_i32 s3, s2, 31
	v_ashrrev_i32_e32 v9, 31, v8
	s_lshl_b64 s[0:1], s[2:3], 10
	v_lshl_add_u64 v[10:11], s[0:1], 0, v[8:9]
	s_or_b32 s22, s2, 1
	s_mov_b32 s23, s3
	v_lshl_add_u64 v[12:13], v[10:11], 2, s[8:9]
	s_lshl_b64 s[0:1], s[22:23], 10
	global_load_dword v41, v[12:13], off
	v_lshl_add_u64 v[12:13], s[0:1], 0, v[8:9]
	s_or_b32 s18, s2, 2
	s_mov_b32 s19, s3
	v_lshl_add_u64 v[14:15], v[12:13], 2, s[8:9]
	v_lshl_add_u64 v[12:13], v[12:13], 1, s[6:7]
	s_lshl_b64 s[0:1], s[18:19], 10
	s_or_b32 s16, s2, 3
	s_mov_b32 s17, s3
	global_load_dword v20, v[14:15], off
	s_or_b32 s14, s2, 4
	global_load_ushort v15, v[12:13], off nt
	v_lshl_add_u64 v[12:13], s[0:1], 0, v[8:9]
	s_lshl_b64 s[0:1], s[16:17], 10
	v_lshl_add_u64 v[18:19], s[0:1], 0, v[8:9]
	s_mov_b32 s15, s3
	v_lshl_add_u64 v[16:17], v[12:13], 2, s[8:9]
	v_lshl_add_u64 v[12:13], v[12:13], 1, s[6:7]
	v_lshl_add_u64 v[22:23], v[18:19], 2, s[8:9]
	v_lshl_add_u64 v[18:19], v[18:19], 1, s[6:7]
	s_lshl_b64 s[0:1], s[14:15], 10
	global_load_dword v16, v[16:17], off
	s_or_b32 s30, s2, 5
	global_load_dword v14, v[22:23], off
	s_mov_b32 s31, s3
	global_load_ushort v13, v[12:13], off nt
	s_or_b32 s26, s2, 6
	global_load_ushort v12, v[18:19], off nt
	v_lshl_add_u64 v[18:19], s[0:1], 0, v[8:9]
	v_lshl_add_u64 v[22:23], v[18:19], 2, s[8:9]
	v_lshl_add_u64 v[18:19], v[18:19], 1, s[6:7]
	s_lshl_b64 s[0:1], s[30:31], 10
	global_load_dword v31, v[22:23], off
	global_load_ushort v24, v[18:19], off nt
	v_lshl_add_u64 v[18:19], s[0:1], 0, v[8:9]
	s_mov_b32 s27, s3
	v_lshl_add_u64 v[22:23], v[18:19], 2, s[8:9]
	v_lshl_add_u64 v[18:19], v[18:19], 1, s[6:7]
	s_lshl_b64 s[0:1], s[26:27], 10
	s_or_b32 s24, s2, 7
	s_mov_b32 s25, s3
	global_load_dword v25, v[22:23], off
	global_load_ushort v21, v[18:19], off nt
	v_lshl_add_u64 v[18:19], s[0:1], 0, v[8:9]
	s_lshl_b64 s[0:1], s[24:25], 10
	v_lshl_add_u64 v[26:27], s[0:1], 0, v[8:9]
	s_or_b32 s20, s2, 8
	s_mov_b32 s21, s3
	v_lshl_add_u64 v[22:23], v[18:19], 2, s[8:9]
	v_lshl_add_u64 v[28:29], v[26:27], 2, s[8:9]
	v_lshl_add_u64 v[26:27], v[26:27], 1, s[6:7]
	s_lshl_b64 s[0:1], s[20:21], 10
	global_load_dword v22, v[22:23], off
	v_lshl_add_u64 v[18:19], v[18:19], 1, s[6:7]
	global_load_ushort v17, v[26:27], off nt
	v_lshl_add_u64 v[26:27], s[0:1], 0, v[8:9]
	s_or_b32 s38, s2, 9
	s_mov_b32 s39, s3
	global_load_ushort v18, v[18:19], off nt
	s_lshl_b64 s[0:1], s[38:39], 10
	global_load_dword v19, v[28:29], off
	v_lshl_add_u64 v[28:29], v[26:27], 2, s[8:9]
	v_lshl_add_u64 v[26:27], v[26:27], 1, s[6:7]
	global_load_dword v37, v[28:29], off
	global_load_ushort v32, v[26:27], off nt
	v_lshl_add_u64 v[26:27], s[0:1], 0, v[8:9]
	s_or_b32 s36, s2, 10
	s_mov_b32 s37, s3
	v_lshl_add_u64 v[28:29], v[26:27], 2, s[8:9]
	v_lshl_add_u64 v[26:27], v[26:27], 1, s[6:7]
	s_lshl_b64 s[0:1], s[36:37], 10
	global_load_dword v33, v[28:29], off
	s_or_b32 s34, s2, 11
	global_load_ushort v28, v[26:27], off nt
	v_lshl_add_u64 v[26:27], s[0:1], 0, v[8:9]
	s_mov_b32 s35, s3
	v_lshl_add_u64 v[34:35], v[26:27], 2, s[8:9]
	v_lshl_add_u64 v[26:27], v[26:27], 1, s[6:7]
	s_lshl_b64 s[0:1], s[34:35], 10
	global_load_dword v29, v[34:35], off
	s_or_b32 s28, s2, 12
	global_load_ushort v26, v[26:27], off nt
	v_lshl_add_u64 v[34:35], s[0:1], 0, v[8:9]
	s_mov_b32 s29, s3
	v_lshl_add_u64 v[38:39], v[34:35], 2, s[8:9]
	v_lshl_add_u64 v[34:35], v[34:35], 1, s[6:7]
	s_lshl_b64 s[0:1], s[28:29], 10
	global_load_dword v27, v[38:39], off
	global_load_ushort v23, v[34:35], off nt
	v_lshl_add_u64 v[34:35], s[0:1], 0, v[8:9]
	s_or_b32 s42, s2, 13
	s_mov_b32 s43, s3
	v_lshl_add_u64 v[38:39], v[34:35], 2, s[8:9]
	v_lshl_add_u64 v[34:35], v[34:35], 1, s[6:7]
	s_lshl_b64 s[0:1], s[42:43], 10
	global_load_dword v40, v[38:39], off
	s_or_b32 s40, s2, 14
	global_load_ushort v38, v[34:35], off nt
	v_lshl_add_u64 v[34:35], s[0:1], 0, v[8:9]
	s_mov_b32 s41, s3
	v_lshl_add_u64 v[42:43], v[34:35], 2, s[8:9]
	v_lshl_add_u64 v[34:35], v[34:35], 1, s[6:7]
	s_lshl_b64 s[0:1], s[40:41], 10
	global_load_dword v39, v[42:43], off
	s_nop 0
	global_load_ushort v35, v[34:35], off nt
	v_lshl_add_u64 v[42:43], s[0:1], 0, v[8:9]
	s_or_b32 s0, s2, 15
	s_mov_b32 s1, s3
	v_lshl_add_u64 v[44:45], v[42:43], 2, s[8:9]
	v_lshl_add_u64 v[42:43], v[42:43], 1, s[6:7]
	s_lshl_b64 s[12:13], s[0:1], 10
	global_load_dword v36, v[44:45], off
	global_load_ushort v34, v[42:43], off nt
	v_lshl_add_u64 v[42:43], s[12:13], 0, v[8:9]
	v_lshl_add_u64 v[44:45], v[42:43], 2, s[8:9]
	v_lshl_add_u64 v[42:43], v[42:43], 1, s[6:7]
	global_load_dword v30, v[44:45], off
	s_ashr_i32 s12, s54, 1
	global_load_ushort v44, v[42:43], off nt
	s_waitcnt vmcnt(0)
	v_lshlrev_b32_e32 v42, 16, v41
	v_mul_f32_e32 v42, 0x3fb8aa3b, v42
	v_exp_f32_e32 v42, v42
	s_and_b32 s13, s12, 63
	s_cmp_eq_u32 s13, 0
	s_cselect_b64 s[46:47], -1, 0
	s_cmp_lg_u32 s13, 0
	v_and_b32_e32 v41, 0xffff0000, v41
	s_cselect_b64 s[44:45], -1, 0
	v_lshl_add_u64 v[8:9], v[8:9], 1, s[10:11]
	v_fmac_f32_e32 v41, 0, v42
	s_and_b64 vcc, exec, s[46:47]
	s_cbranch_vccz .LBB0_741
	v_lshl_add_u64 v[10:11], v[10:11], 1, s[6:7]
	global_load_ushort v10, v[10:11], off nt
	s_lshl_b64 s[2:3], s[2:3], 11
	s_waitcnt vmcnt(0)
	v_lshlrev_b32_e32 v10, 16, v10
	v_mul_f32_e32 v10, v41, v10
	v_cvt_pk_bf16_f32 v42, v10, s0
	v_lshl_add_u64 v[10:11], v[8:9], 0, s[2:3]
	global_store_short v[10:11], v42, off

; DI bf16_t f2bf(float f) { return (bf16_t)(pk_bf16(f, 0.f) & 0xffffu); }
; DI float bf2f(unsigned b) { return __uint_as_float(b << 16); }
; DI float bflo(unsigned p) { return __uint_as_float(p << 16); }
; DI float bfhi(unsigned p) { return __uint_as_float(p & 0xffff0000u); }
; DI void phase_scan2(const Ctx& c) {
;     ...
; #pragma unroll 1
;         for (int t = 0; t < 256; t += 32) {
;             unsigned w[32]; unsigned short y[32];
; #pragma unroll
;             for (int k = 0; k < 32; ++k) { w[k] = AB[(row0 + t + k) * 1024 + ch]; y[k] = YB[(row0 + t + k) * 1024 + ch]; }
; #pragma unroll
;             for (int k = 0; k < 32; ++k) { h = __expf(bflo(w[k])) * h + bfhi(w[k]); Z[(row0 + t + k) * 1024 + ch] = f2bf(bf2f(y[k]) * h); }
.LBB0_807:
	v_lshl_add_u64 v[18:19], s[4:5], 0, v[10:11]
	v_add_co_u32_e32 v52, vcc, 0x3e4c3000, v18
	v_lshl_add_u64 v[22:23], s[4:5], 0, v[12:13]
	s_nop 0
	v_addc_co_u32_e32 v53, vcc, 0, v19, vcc
	v_add_co_u32_e32 v54, vcc, 0x3e4c4000, v18
	global_load_dword v51, v[22:23], off
	global_load_dword v58, v[52:53], off offset:2048
	v_addc_co_u32_e32 v55, vcc, 0, v19, vcc
	v_add_co_u32_e32 v52, vcc, 0x3e4c5000, v18
	v_lshl_add_u64 v[20:21], s[4:5], 0, v[14:15]
	s_nop 0
	v_addc_co_u32_e32 v53, vcc, 0, v19, vcc
	v_add_co_u32_e32 v56, vcc, 0x3e4c6000, v18
	global_load_dword v59, v[54:55], off offset:2048
	global_load_dword v60, v[52:53], off offset:2048
	v_addc_co_u32_e32 v57, vcc, 0, v19, vcc
	v_add_co_u32_e32 v52, vcc, 0x3e4c7000, v18
	v_lshl_add_u64 v[16:17], s[4:5], 0, v[8:9]
	s_nop 0
	v_addc_co_u32_e32 v53, vcc, 0, v19, vcc
	v_add_co_u32_e32 v54, vcc, 0x3e4c8000, v18
	global_load_dword v61, v[56:57], off offset:2048
	global_load_dword v62, v[52:53], off offset:2048
	v_addc_co_u32_e32 v55, vcc, 0, v19, vcc
	v_add_co_u32_e32 v52, vcc, 0x3e4c9000, v18
	global_load_dword v63, v[54:55], off offset:2048
	global_load_ushort v64, v[20:21], off nt
	v_addc_co_u32_e32 v53, vcc, 0, v19, vcc
	v_add_co_u32_e32 v56, vcc, 0x3e4ca000, v18
	s_add_i32 s0, s0, 32
	s_nop 0
	v_addc_co_u32_e32 v57, vcc, 0, v19, vcc
	v_add_co_u32_e32 v20, vcc, 0x3e4cb000, v18
	global_load_dword v65, v[52:53], off offset:2048
	s_nop 0
	global_load_dword v56, v[56:57], off offset:2048
	v_addc_co_u32_e32 v21, vcc, 0, v19, vcc
	v_add_co_u32_e32 v52, vcc, 0x3e4cc000, v18
	s_mov_b32 s1, 0x3a444000
	s_nop 0
	v_addc_co_u32_e32 v53, vcc, 0, v19, vcc
	v_add_co_u32_e32 v54, vcc, 0x3e4cd000, v18
	global_load_dword v57, v[20:21], off offset:2048
	global_load_dword v66, v[52:53], off offset:2048
	v_addc_co_u32_e32 v55, vcc, 0, v19, vcc
	v_add_co_u32_e32 v20, vcc, 0x3e4ce000, v18
	v_add_co_u32_e64 v48, s[2:3], s1, v16
	s_nop 0
	v_addc_co_u32_e32 v21, vcc, 0, v19, vcc
	v_add_co_u32_e32 v52, vcc, 0x3e4cf000, v18
	global_load_dword v67, v[54:55], off offset:2048
	global_load_dword v68, v[20:21], off offset:2048
	v_addc_co_u32_e32 v53, vcc, 0, v19, vcc
	v_add_co_u32_e32 v20, vcc, 0x3e4d0000, v18
	s_mov_b32 s12, 0x3a445000
	s_nop 0
	v_addc_co_u32_e32 v21, vcc, 0, v19, vcc
	v_add_co_u32_e32 v54, vcc, 0x3e4d1000, v18
	global_load_dword v69, v[52:53], off offset:2048
	global_load_dword v70, v[20:21], off offset:2048
	v_addc_co_u32_e32 v55, vcc, 0, v19, vcc
	v_add_co_u32_e32 v20, vcc, 0x3e4d2000, v18
	v_addc_co_u32_e64 v49, s[2:3], 0, v17, s[2:3]
	s_nop 0
	v_addc_co_u32_e32 v21, vcc, 0, v19, vcc
	v_add_co_u32_e32 v52, vcc, 0x3e4d3000, v18
	global_load_dword v71, v[54:55], off offset:2048
	global_load_dword v72, v[20:21], off offset:2048
	v_addc_co_u32_e32 v53, vcc, 0, v19, vcc
	v_add_co_u32_e32 v20, vcc, 0x3e4d4000, v18
	v_add_co_u32_e64 v46, s[2:3], s12, v16
	s_nop 0
	v_addc_co_u32_e32 v21, vcc, 0, v19, vcc
	v_add_co_u32_e32 v54, vcc, 0x3e4d5000, v18
	global_load_dword v73, v[52:53], off offset:2048
	global_load_dword v74, v[20:21], off offset:2048
	v_addc_co_u32_e32 v55, vcc, 0, v19, vcc
	v_add_co_u32_e32 v20, vcc, 0x3e4d6000, v18
	s_waitcnt vmcnt(17)
	v_lshlrev_b32_e32 v117, 16, v59
	v_addc_co_u32_e32 v21, vcc, 0, v19, vcc
	v_add_co_u32_e32 v52, vcc, 0x3e4d7000, v18
	global_load_dword v75, v[54:55], off offset:2048
	global_load_dword v76, v[20:21], off offset:2048
	v_addc_co_u32_e32 v53, vcc, 0, v19, vcc
	v_add_co_u32_e32 v20, vcc, 0x3e4d8000, v18
	v_mul_f32_e32 v117, 0x3fb8aa3b, v117
	s_nop 0
	v_addc_co_u32_e32 v21, vcc, 0, v19, vcc
	v_add_co_u32_e32 v54, vcc, 0x3e4d9000, v18
	global_load_dword v77, v[52:53], off offset:2048
	global_load_dword v78, v[20:21], off offset:2048
	v_addc_co_u32_e32 v55, vcc, 0, v19, vcc
	v_add_co_u32_e32 v20, vcc, 0x3e4da000, v18
	s_waitcnt vmcnt(20)
	v_lshlrev_b32_e32 v118, 16, v60
	v_addc_co_u32_e32 v21, vcc, 0, v19, vcc
	v_add_co_u32_e32 v52, vcc, 0x3e4db000, v18
	global_load_dword v79, v[54:55], off offset:2048
	global_load_dword v80, v[20:21], off offset:2048
	v_addc_co_u32_e32 v53, vcc, 0, v19, vcc
	v_add_co_u32_e32 v20, vcc, 0x3e4dc000, v18
	v_exp_f32_e32 v117, v117
	s_nop 0
	v_addc_co_u32_e32 v21, vcc, 0, v19, vcc
	v_add_co_u32_e32 v54, vcc, 0x3e4dd000, v18
	global_load_dword v81, v[52:53], off offset:2048
	global_load_dword v82, v[20:21], off offset:2048
	v_addc_co_u32_e32 v55, vcc, 0, v19, vcc
	v_add_co_u32_e32 v20, vcc, 0x3e4de000, v18
	v_mul_f32_e32 v118, 0x3fb8aa3b, v118
	s_nop 0
	v_addc_co_u32_e32 v21, vcc, 0, v19, vcc
	v_add_co_u32_e32 v52, vcc, 0x3e4df000, v18
	global_load_dword v83, v[54:55], off offset:2048
	global_load_dword v84, v[20:21], off offset:2048
	v_addc_co_u32_e32 v53, vcc, 0, v19, vcc
	v_add_co_u32_e32 v20, vcc, 0x3e4e0000, v18
	s_waitcnt vmcnt(25)
	v_lshlrev_b32_e32 v119, 16, v61
	v_addc_co_u32_e32 v21, vcc, 0, v19, vcc
	v_add_co_u32_e32 v18, vcc, 0x3e4e1000, v18
	global_load_dword v85, v[52:53], off offset:2048
	global_load_dword v86, v[20:21], off offset:2048
	v_addc_co_u32_e32 v19, vcc, 0, v19, vcc
	v_add_co_u32_e32 v20, vcc, 0x3a442000, v16
	global_load_dword v87, v[18:19], off offset:2048
	s_nop 0
	v_addc_co_u32_e32 v21, vcc, 0, v17, vcc
	v_add_co_u32_e32 v18, vcc, 0x2e2c3000, v16
	s_waitcnt vmcnt(25)
; DI bf16_t f2bf(float f) { return (bf16_t)(pk_bf16(f, 0.f) & 0xffffu); }
; DI float bf2f(unsigned b) { return __uint_as_float(b << 16); }
; DI float bflo(unsigned p) { return __uint_as_float(p << 16); }
; DI float bfhi(unsigned p) { return __uint_as_float(p & 0xffff0000u); }
; DI void phase_scan2(const Ctx& c) {
;     ...
; #pragma unroll 1
;         for (int t = 0; t < 256; t += 32) {
;             unsigned w[32]; unsigned short y[32];
; #pragma unroll
;             for (int k = 0; k < 32; ++k) { w[k] = AB[(row0 + t + k) * 1024 + ch]; y[k] = YB[(row0 + t + k) * 1024 + ch]; }
; #pragma unroll
;             for (int k = 0; k < 32; ++k) { h = __expf(bflo(w[k])) * h + bfhi(w[k]); Z[(row0 + t + k) * 1024 + ch] = f2bf(bf2f(y[k]) * h); }
	v_lshlrev_b32_e32 v64, 16, v64
	v_addc_co_u32_e32 v19, vcc, 0, v17, vcc
	v_add_co_u32_e32 v52, vcc, 0x2e2c4000, v16
	v_and_b32_e32 v59, 0xffff0000, v59
	s_nop 0
	v_addc_co_u32_e32 v53, vcc, 0, v17, vcc
	v_add_co_u32_e32 v54, vcc, 0x2e2c5000, v16
	global_load_ushort v88, v[18:19], off nt
	global_load_ushort v89, v[18:19], off offset:2048 nt
	global_load_ushort v90, v[52:53], off nt
	global_load_ushort v91, v[52:53], off offset:2048 nt
	v_addc_co_u32_e32 v55, vcc, 0, v17, vcc
	v_add_co_u32_e32 v18, vcc, 0x2e2c6000, v16
	v_and_b32_e32 v60, 0xffff0000, v60
	s_nop 0
	v_addc_co_u32_e32 v19, vcc, 0, v17, vcc
	v_add_co_u32_e32 v52, vcc, 0x2e2c7000, v16
	global_load_ushort v92, v[54:55], off nt
	global_load_ushort v93, v[54:55], off offset:2048 nt
	global_load_ushort v94, v[18:19], off nt
	global_load_ushort v95, v[18:19], off offset:2048 nt
	v_addc_co_u32_e32 v53, vcc, 0, v17, vcc
	v_add_co_u32_e32 v18, vcc, 0x2e2c8000, v16
	v_and_b32_e32 v61, 0xffff0000, v61
	s_nop 0
	v_addc_co_u32_e32 v19, vcc, 0, v17, vcc
	v_add_co_u32_e32 v54, vcc, 0x2e2c9000, v16
	global_load_ushort v96, v[52:53], off nt
	global_load_ushort v97, v[52:53], off offset:2048 nt
	global_load_ushort v98, v[18:19], off nt
	global_load_ushort v99, v[18:19], off offset:2048 nt
	v_addc_co_u32_e32 v55, vcc, 0, v17, vcc
	v_add_co_u32_e32 v18, vcc, 0x2e2ca000, v16
	s_mov_b32 s13, 0x3a446000
	s_nop 0
	v_addc_co_u32_e32 v19, vcc, 0, v17, vcc
	v_add_co_u32_e32 v52, vcc, 0x2e2cb000, v16
	global_load_ushort v100, v[54:55], off nt
	global_load_ushort v101, v[54:55], off offset:2048 nt
	global_load_ushort v102, v[18:19], off nt
	global_load_ushort v103, v[18:19], off offset:2048 nt
	v_addc_co_u32_e32 v53, vcc, 0, v17, vcc
	v_add_co_u32_e32 v18, vcc, 0x2e2cc000, v16
	v_addc_co_u32_e64 v47, s[2:3], 0, v17, s[2:3]
	s_nop 0
	v_addc_co_u32_e32 v19, vcc, 0, v17, vcc
	v_add_co_u32_e32 v54, vcc, 0x2e2cd000, v16
	global_load_ushort v104, v[52:53], off nt
	global_load_ushort v105, v[52:53], off offset:2048 nt
	global_load_ushort v106, v[18:19], off nt
	global_load_ushort v107, v[18:19], off offset:2048 nt
	v_addc_co_u32_e32 v55, vcc, 0, v17, vcc
	v_add_co_u32_e32 v18, vcc, 0x2e2ce000, v16
	v_add_co_u32_e64 v44, s[2:3], s13, v16
	s_nop 0
	v_addc_co_u32_e32 v19, vcc, 0, v17, vcc
	v_add_co_u32_e32 v52, vcc, 0x2e2cf000, v16
	global_load_ushort v108, v[54:55], off nt
	global_load_ushort v109, v[54:55], off offset:2048 nt
	global_load_ushort v110, v[18:19], off nt
	global_load_ushort v111, v[18:19], off offset:2048 nt
	v_addc_co_u32_e32 v53, vcc, 0, v17, vcc
	v_add_co_u32_e32 v18, vcc, 0x2e2d0000, v16
	s_mov_b32 s14, 0x3a447000
	s_nop 0
	v_addc_co_u32_e32 v19, vcc, 0, v17, vcc
	v_add_co_u32_e32 v54, vcc, 0x2e2d1000, v16
	global_load_ushort v112, v[52:53], off nt
	global_load_ushort v113, v[52:53], off offset:2048 nt
	global_load_ushort v114, v[18:19], off nt
	global_load_ushort v115, v[18:19], off offset:2048 nt
	v_addc_co_u32_e32 v55, vcc, 0, v17, vcc
	v_add_co_u32_e32 v18, vcc, 0x2e2d2000, v16
	v_addc_co_u32_e64 v45, s[2:3], 0, v17, s[2:3]
	s_nop 0
	v_addc_co_u32_e32 v19, vcc, 0, v17, vcc
	global_load_ushort v116, v[54:55], off nt
	s_nop 0
	global_load_ushort v54, v[54:55], off offset:2048 nt
	s_nop 0
	global_load_ushort v18, v[18:19], off nt
	v_lshlrev_b32_e32 v19, 16, v51
	v_mul_f32_e32 v19, 0x3fb8aa3b, v19
	v_exp_f32_e32 v19, v19
	v_lshlrev_b32_e32 v55, 16, v58
	v_mul_f32_e32 v55, 0x3fb8aa3b, v55
	v_exp_f32_e32 v55, v55
	v_and_b32_e32 v51, 0xffff0000, v51
	v_fmac_f32_e32 v51, v50, v19
	v_exp_f32_e32 v19, v118
	v_mul_f32_e32 v50, 0x3fb8aa3b, v119
	v_lshlrev_b32_e32 v118, 16, v62
	v_and_b32_e32 v58, 0xffff0000, v58
	v_exp_f32_e32 v50, v50
	v_mul_f32_e32 v118, 0x3fb8aa3b, v118
	v_lshlrev_b32_e32 v119, 16, v63
	v_mul_f32_e32 v64, v51, v64
	v_fmac_f32_e32 v58, v51, v55
	v_exp_f32_e32 v51, v118
	v_mul_f32_e32 v55, 0x3fb8aa3b, v119
	s_waitcnt vmcnt(55)
	v_lshlrev_b32_e32 v118, 16, v65
	v_cvt_pk_bf16_f32 v64, v64, s0
	v_fmac_f32_e32 v59, v58, v117
	v_exp_f32_e32 v55, v55
	v_mul_f32_e32 v117, 0x3fb8aa3b, v118
	s_waitcnt vmcnt(54)
	v_lshlrev_b32_e32 v118, 16, v56
	global_store_short v[20:21], v64, off offset:2048
	v_fmac_f32_e32 v60, v59, v19
	v_exp_f32_e32 v19, v117
	v_mul_f32_e32 v20, 0x3fb8aa3b, v118
	s_waitcnt vmcnt(54)
	v_lshlrev_b32_e32 v21, 16, v57
	v_and_b32_e32 v62, 0xffff0000, v62
	v_fmac_f32_e32 v61, v60, v50
	v_exp_f32_e32 v20, v20
	v_mul_f32_e32 v21, 0x3fb8aa3b, v21
	s_waitcnt vmcnt(53)
	v_lshlrev_b32_e32 v50, 16, v66
	v_and_b32_e32 v63, 0xffff0000, v63
	v_fmac_f32_e32 v62, v61, v51
	v_exp_f32_e32 v21, v21
	v_mul_f32_e32 v50, 0x3fb8aa3b, v50
	s_waitcnt vmcnt(52)
	v_lshlrev_b32_e32 v51, 16, v67
	v_and_b32_e32 v65, 0xffff0000, v65
	v_fmac_f32_e32 v63, v62, v55
	v_exp_f32_e32 v50, v50
	v_mul_f32_e32 v51, 0x3fb8aa3b, v51
	s_waitcnt vmcnt(51)
	v_lshlrev_b32_e32 v55, 16, v68
	v_and_b32_e32 v56, 0xffff0000, v56
	v_fmac_f32_e32 v65, v63, v19
	v_exp_f32_e32 v19, v51
	v_mul_f32_e32 v51, 0x3fb8aa3b, v55
	s_waitcnt vmcnt(50)
	v_lshlrev_b32_e32 v55, 16, v69
	v_and_b32_e32 v57, 0xffff0000, v57
	v_fmac_f32_e32 v56, v65, v20
	v_exp_f32_e32 v20, v51
	v_mul_f32_e32 v51, 0x3fb8aa3b, v55
	s_waitcnt vmcnt(49)
	v_lshlrev_b32_e32 v55, 16, v70
	v_and_b32_e32 v64, 0xffff0000, v66
	v_fmac_f32_e32 v57, v56, v21
	v_exp_f32_e32 v21, v51
	v_mul_f32_e32 v51, 0x3fb8aa3b, v55
	s_waitcnt vmcnt(48)
	v_lshlrev_b32_e32 v55, 16, v71
	v_and_b32_e32 v66, 0xffff0000, v67
	v_fmac_f32_e32 v64, v57, v50
	v_exp_f32_e32 v50, v51
	v_mul_f32_e32 v51, 0x3fb8aa3b, v55
	s_waitcnt vmcnt(47)
	v_lshlrev_b32_e32 v55, 16, v72
	v_and_b32_e32 v67, 0xffff0000, v68
	v_fmac_f32_e32 v66, v64, v19
	v_exp_f32_e32 v19, v51
	v_mul_f32_e32 v51, 0x3fb8aa3b, v55
	s_waitcnt vmcnt(46)
; DI bf16_t f2bf(float f) { return (bf16_t)(pk_bf16(f, 0.f) & 0xffffu); }
; DI float bf2f(unsigned b) { return __uint_as_float(b << 16); }
; DI float bflo(unsigned p) { return __uint_as_float(p << 16); }
; DI float bfhi(unsigned p) { return __uint_as_float(p & 0xffff0000u); }
; DI void phase_scan2(const Ctx& c) {
;     ...
; #pragma unroll 1
;         for (int t = 0; t < 256; t += 32) {
;             unsigned w[32]; unsigned short y[32];
; #pragma unroll
;             for (int k = 0; k < 32; ++k) { w[k] = AB[(row0 + t + k) * 1024 + ch]; y[k] = YB[(row0 + t + k) * 1024 + ch]; }
; #pragma unroll
;             for (int k = 0; k < 32; ++k) { h = __expf(bflo(w[k])) * h + bfhi(w[k]); Z[(row0 + t + k) * 1024 + ch] = f2bf(bf2f(y[k]) * h); }
	v_lshlrev_b32_e32 v55, 16, v73
	v_and_b32_e32 v68, 0xffff0000, v69
	v_fmac_f32_e32 v67, v66, v20
	v_exp_f32_e32 v20, v51
	v_mul_f32_e32 v51, 0x3fb8aa3b, v55
	s_waitcnt vmcnt(45)
	v_lshlrev_b32_e32 v55, 16, v74
	v_and_b32_e32 v69, 0xffff0000, v70
	v_fmac_f32_e32 v68, v67, v21
	v_exp_f32_e32 v21, v51
	v_mul_f32_e32 v51, 0x3fb8aa3b, v55
	s_waitcnt vmcnt(44)
	v_lshlrev_b32_e32 v55, 16, v75
	v_and_b32_e32 v70, 0xffff0000, v71
	v_fmac_f32_e32 v69, v68, v50
	v_exp_f32_e32 v50, v51
	v_mul_f32_e32 v51, 0x3fb8aa3b, v55
	s_waitcnt vmcnt(43)
	v_lshlrev_b32_e32 v55, 16, v76
	v_and_b32_e32 v71, 0xffff0000, v72
	v_fmac_f32_e32 v70, v69, v19
	v_exp_f32_e32 v19, v51
	v_mul_f32_e32 v51, 0x3fb8aa3b, v55
	s_waitcnt vmcnt(42)
	v_lshlrev_b32_e32 v55, 16, v77
	v_and_b32_e32 v72, 0xffff0000, v73
	v_fmac_f32_e32 v71, v70, v20
	v_exp_f32_e32 v20, v51
	v_mul_f32_e32 v51, 0x3fb8aa3b, v55
	s_waitcnt vmcnt(41)
	v_lshlrev_b32_e32 v55, 16, v78
	v_and_b32_e32 v73, 0xffff0000, v74
	v_fmac_f32_e32 v72, v71, v21
	v_exp_f32_e32 v21, v51
	v_mul_f32_e32 v51, 0x3fb8aa3b, v55
	s_waitcnt vmcnt(40)
	v_lshlrev_b32_e32 v55, 16, v79
	v_and_b32_e32 v74, 0xffff0000, v75
	v_fmac_f32_e32 v73, v72, v50
	v_exp_f32_e32 v50, v51
	v_mul_f32_e32 v51, 0x3fb8aa3b, v55
	s_waitcnt vmcnt(39)
	v_lshlrev_b32_e32 v55, 16, v80
	v_and_b32_e32 v75, 0xffff0000, v76
	v_fmac_f32_e32 v74, v73, v19
	v_exp_f32_e32 v19, v51
	v_mul_f32_e32 v51, 0x3fb8aa3b, v55
	s_waitcnt vmcnt(38)
	v_lshlrev_b32_e32 v55, 16, v81
	v_add_co_u32_e64 v42, s[2:3], s14, v16
	v_and_b32_e32 v76, 0xffff0000, v77
	v_fmac_f32_e32 v75, v74, v20
	v_exp_f32_e32 v20, v51
	v_mul_f32_e32 v51, 0x3fb8aa3b, v55
	s_waitcnt vmcnt(37)
	v_lshlrev_b32_e32 v55, 16, v82
	s_mov_b32 s15, 0x3a448000
	v_addc_co_u32_e64 v43, s[2:3], 0, v17, s[2:3]
	v_and_b32_e32 v77, 0xffff0000, v78
	v_fmac_f32_e32 v76, v75, v21
	v_exp_f32_e32 v21, v51
	v_mul_f32_e32 v51, 0x3fb8aa3b, v55
	s_waitcnt vmcnt(36)
	v_lshlrev_b32_e32 v55, 16, v83
	v_add_co_u32_e64 v40, s[2:3], s15, v16
	v_and_b32_e32 v78, 0xffff0000, v79
	v_fmac_f32_e32 v77, v76, v50
	v_exp_f32_e32 v51, v51
	v_mul_f32_e32 v50, 0x3fb8aa3b, v55
	s_waitcnt vmcnt(35)
	v_lshlrev_b32_e32 v55, 16, v84
	s_mov_b32 s16, 0x3a449000
	v_addc_co_u32_e64 v41, s[2:3], 0, v17, s[2:3]
	v_and_b32_e32 v79, 0xffff0000, v80
	v_fmac_f32_e32 v78, v77, v19
	v_exp_f32_e32 v19, v50
	v_mul_f32_e32 v50, 0x3fb8aa3b, v55
	s_waitcnt vmcnt(34)
	v_lshlrev_b32_e32 v55, 16, v85
	v_add_co_u32_e64 v38, s[2:3], s16, v16
	v_and_b32_e32 v80, 0xffff0000, v81
	v_fmac_f32_e32 v79, v78, v20
	v_exp_f32_e32 v20, v50
	v_mul_f32_e32 v50, 0x3fb8aa3b, v55
	s_waitcnt vmcnt(33)
	v_lshlrev_b32_e32 v55, 16, v86
	s_mov_b32 s17, 0x3a44a000
	v_addc_co_u32_e64 v39, s[2:3], 0, v17, s[2:3]
	v_and_b32_e32 v81, 0xffff0000, v82
	v_and_b32_e32 v82, 0xffff0000, v83
	v_and_b32_e32 v83, 0xffff0000, v84
	v_and_b32_e32 v84, 0xffff0000, v85
	v_and_b32_e32 v85, 0xffff0000, v86
	v_fmac_f32_e32 v80, v79, v21
	v_exp_f32_e32 v21, v50
	v_mul_f32_e32 v55, 0x3fb8aa3b, v55
	s_waitcnt vmcnt(32)
	v_lshlrev_b32_e32 v86, 16, v87
	v_add_co_u32_e64 v36, s[2:3], s17, v16
	v_and_b32_e32 v50, 0xffff0000, v87
	v_fmac_f32_e32 v81, v80, v51
	v_exp_f32_e32 v51, v55
	v_mul_f32_e32 v55, 0x3fb8aa3b, v86
	s_waitcnt vmcnt(31)
	v_lshlrev_b32_e32 v86, 16, v88
	s_waitcnt vmcnt(30)
	v_lshlrev_b32_e32 v87, 16, v89
	s_mov_b32 s18, 0x3a44b000
	v_addc_co_u32_e64 v37, s[2:3], 0, v17, s[2:3]
	v_add_co_u32_e32 v52, vcc, 0x3a443000, v16
	v_fmac_f32_e32 v82, v81, v19
	v_exp_f32_e32 v19, v55
	v_mul_f32_e32 v55, v58, v86
	v_mul_f32_e32 v58, v59, v87
	s_waitcnt vmcnt(29)
	v_lshlrev_b32_e32 v59, 16, v90
	s_waitcnt vmcnt(28)
	v_lshlrev_b32_e32 v86, 16, v91
	v_add_co_u32_e64 v34, s[2:3], s18, v16
	v_addc_co_u32_e32 v53, vcc, 0, v17, vcc
	v_fmac_f32_e32 v83, v82, v20
	v_cvt_pk_bf16_f32 v20, v55, s0
	v_cvt_pk_bf16_f32 v55, v58, s0
	v_mul_f32_e32 v58, v60, v59
	v_mul_f32_e32 v59, v61, v86
	s_waitcnt vmcnt(27)
	v_lshlrev_b32_e32 v60, 16, v92
	s_waitcnt vmcnt(26)
	v_lshlrev_b32_e32 v61, 16, v93
	s_mov_b32 s19, 0x3a44c000
	v_addc_co_u32_e64 v35, s[2:3], 0, v17, s[2:3]
	v_fmac_f32_e32 v84, v83, v21
	global_store_short v[52:53], v20, off
	global_store_short v[52:53], v55, off offset:2048
	v_cvt_pk_bf16_f32 v20, v58, s0
	v_cvt_pk_bf16_f32 v21, v59, s0
	v_mul_f32_e32 v52, v62, v60
	v_mul_f32_e32 v53, v63, v61
	s_waitcnt vmcnt(27)
	v_lshlrev_b32_e32 v55, 16, v94
	v_add_co_u32_e64 v32, s[2:3], s19, v16
	s_waitcnt vmcnt(26)
	v_lshlrev_b32_e32 v58, 16, v95
	v_fmac_f32_e32 v85, v84, v51
	global_store_short v[46:47], v20, off offset:-4096
	global_store_short v[48:49], v21, off offset:2048
	v_cvt_pk_bf16_f32 v20, v52, s0
	v_cvt_pk_bf16_f32 v21, v53, s0
	v_mul_f32_e32 v48, v65, v55
	s_waitcnt vmcnt(27)
	v_lshlrev_b32_e32 v51, 16, v96
	s_mov_b32 s20, 0x3a44d000
	v_addc_co_u32_e64 v33, s[2:3], 0, v17, s[2:3]
	v_mul_f32_e32 v49, v56, v58
	s_waitcnt vmcnt(26)
; DI bf16_t f2bf(float f) { return (bf16_t)(pk_bf16(f, 0.f) & 0xffffu); }
; DI float bf2f(unsigned b) { return __uint_as_float(b << 16); }
; DI float bflo(unsigned p) { return __uint_as_float(p << 16); }
; DI float bfhi(unsigned p) { return __uint_as_float(p & 0xffff0000u); }
; DI void phase_scan2(const Ctx& c) {
;     ...
; #pragma unroll 1
;         for (int t = 0; t < 256; t += 32) {
;             unsigned w[32]; unsigned short y[32];
; #pragma unroll
;             for (int k = 0; k < 32; ++k) { w[k] = AB[(row0 + t + k) * 1024 + ch]; y[k] = YB[(row0 + t + k) * 1024 + ch]; }
; #pragma unroll
;             for (int k = 0; k < 32; ++k) { h = __expf(bflo(w[k])) * h + bfhi(w[k]); Z[(row0 + t + k) * 1024 + ch] = f2bf(bf2f(y[k]) * h); }
;         }
;     }
	v_lshlrev_b32_e32 v52, 16, v97
	v_fmac_f32_e32 v50, v85, v19
	global_store_short v[46:47], v20, off
	global_store_short v[46:47], v21, off offset:2048
	v_cvt_pk_bf16_f32 v19, v48, s0
	v_mul_f32_e32 v21, v57, v51
	s_waitcnt vmcnt(27)
	v_lshlrev_b32_e32 v47, 16, v98
	v_add_co_u32_e64 v30, s[2:3], s20, v16
	v_cvt_pk_bf16_f32 v20, v49, s0
	v_mul_f32_e32 v46, v64, v52
	s_waitcnt vmcnt(26)
	v_lshlrev_b32_e32 v48, 16, v99
	global_store_short v[42:43], v19, off offset:-4096
	global_store_short v[44:45], v20, off offset:2048
	v_cvt_pk_bf16_f32 v19, v21, s0
	v_mul_f32_e32 v21, v66, v47
	s_waitcnt vmcnt(27)
	v_lshlrev_b32_e32 v45, 16, v100
	s_mov_b32 s21, 0x3a44e000
	v_addc_co_u32_e64 v31, s[2:3], 0, v17, s[2:3]
	v_cvt_pk_bf16_f32 v20, v46, s0
	v_mul_f32_e32 v44, v67, v48
	s_waitcnt vmcnt(26)
	v_lshlrev_b32_e32 v46, 16, v101
	global_store_short v[42:43], v19, off
	global_store_short v[42:43], v20, off offset:2048
	v_cvt_pk_bf16_f32 v19, v21, s0
	v_mul_f32_e32 v21, v68, v45
	s_waitcnt vmcnt(27)
	v_lshlrev_b32_e32 v43, 16, v102
	v_add_co_u32_e64 v28, s[2:3], s21, v16
	v_cvt_pk_bf16_f32 v20, v44, s0
	v_mul_f32_e32 v42, v69, v46
	s_waitcnt vmcnt(26)
	v_lshlrev_b32_e32 v44, 16, v103
	global_store_short v[38:39], v19, off offset:-4096
	global_store_short v[40:41], v20, off offset:2048
	v_cvt_pk_bf16_f32 v19, v21, s0
	v_mul_f32_e32 v21, v70, v43
	s_waitcnt vmcnt(27)
	v_lshlrev_b32_e32 v41, 16, v104
	s_mov_b32 s22, 0x3a44f000
	v_addc_co_u32_e64 v29, s[2:3], 0, v17, s[2:3]
	v_cvt_pk_bf16_f32 v20, v42, s0
	v_mul_f32_e32 v40, v71, v44
	s_waitcnt vmcnt(26)
	v_lshlrev_b32_e32 v42, 16, v105
	global_store_short v[38:39], v19, off
	global_store_short v[38:39], v20, off offset:2048
	v_cvt_pk_bf16_f32 v19, v21, s0
	v_mul_f32_e32 v21, v72, v41
	s_waitcnt vmcnt(27)
	v_lshlrev_b32_e32 v39, 16, v106
	v_add_co_u32_e64 v26, s[2:3], s22, v16
	v_cvt_pk_bf16_f32 v20, v40, s0
	v_mul_f32_e32 v38, v73, v42
	s_waitcnt vmcnt(26)
	v_lshlrev_b32_e32 v40, 16, v107
	global_store_short v[34:35], v19, off offset:-4096
	global_store_short v[36:37], v20, off offset:2048
	v_cvt_pk_bf16_f32 v19, v21, s0
	v_mul_f32_e32 v21, v74, v39
	s_waitcnt vmcnt(27)
	v_lshlrev_b32_e32 v37, 16, v108
	s_mov_b32 s23, 0x3a450000
	v_addc_co_u32_e64 v27, s[2:3], 0, v17, s[2:3]
	v_cvt_pk_bf16_f32 v20, v38, s0
	v_mul_f32_e32 v36, v75, v40
	s_waitcnt vmcnt(26)
	v_lshlrev_b32_e32 v38, 16, v109
	global_store_short v[34:35], v19, off
	global_store_short v[34:35], v20, off offset:2048
	v_cvt_pk_bf16_f32 v19, v21, s0
	v_mul_f32_e32 v21, v76, v37
	s_waitcnt vmcnt(27)
	v_lshlrev_b32_e32 v35, 16, v110
	v_add_co_u32_e64 v24, s[2:3], s23, v16
	v_cvt_pk_bf16_f32 v20, v36, s0
	v_mul_f32_e32 v34, v77, v38
	s_waitcnt vmcnt(26)
	v_lshlrev_b32_e32 v36, 16, v111
	global_store_short v[30:31], v19, off offset:-4096
	global_store_short v[32:33], v20, off offset:2048
	v_cvt_pk_bf16_f32 v19, v21, s0
	v_mul_f32_e32 v21, v78, v35
	s_waitcnt vmcnt(27)
	v_lshlrev_b32_e32 v33, 16, v112
	s_mov_b32 s24, 0x3a451000
	v_addc_co_u32_e64 v25, s[2:3], 0, v17, s[2:3]
	v_cvt_pk_bf16_f32 v20, v34, s0
	v_mul_f32_e32 v32, v79, v36
	s_waitcnt vmcnt(26)
	v_lshlrev_b32_e32 v34, 16, v113
	global_store_short v[30:31], v19, off
	global_store_short v[30:31], v20, off offset:2048
	v_cvt_pk_bf16_f32 v19, v21, s0
	v_mul_f32_e32 v21, v80, v33
	s_waitcnt vmcnt(27)
	v_lshlrev_b32_e32 v31, 16, v114
	v_add_co_u32_e64 v22, s[2:3], s24, v16
	v_cvt_pk_bf16_f32 v20, v32, s0
	v_mul_f32_e32 v30, v81, v34
	s_waitcnt vmcnt(26)
	v_lshlrev_b32_e32 v32, 16, v115
	global_store_short v[26:27], v19, off offset:-4096
	global_store_short v[28:29], v20, off offset:2048
	v_cvt_pk_bf16_f32 v19, v21, s0
	v_mul_f32_e32 v21, v82, v31
	s_waitcnt vmcnt(27)
	v_lshlrev_b32_e32 v29, 16, v116
	s_waitcnt vmcnt(25)
	v_lshlrev_b32_e32 v18, 16, v18
	v_addc_co_u32_e64 v23, s[2:3], 0, v17, s[2:3]
	v_add_co_u32_e32 v16, vcc, 0x3a452000, v16
	v_cvt_pk_bf16_f32 v20, v30, s0
	v_mul_f32_e32 v28, v83, v32
	v_lshlrev_b32_e32 v30, 16, v54
	global_store_short v[26:27], v19, off
	global_store_short v[26:27], v20, off offset:2048
	v_cvt_pk_bf16_f32 v19, v21, s0
	v_mul_f32_e32 v21, v84, v29
	v_mul_f32_e32 v18, v50, v18
	v_lshl_add_u64 v[8:9], v[8:9], 0, s[76:77]
	v_lshl_add_u64 v[10:11], v[10:11], 0, s[78:79]
	v_lshl_add_u64 v[12:13], v[12:13], 0, s[78:79]
	v_lshl_add_u64 v[14:15], v[14:15], 0, s[76:77]
	s_cmpk_gt_u32 s0, 0xdf
	v_addc_co_u32_e32 v17, vcc, 0, v17, vcc
	v_cvt_pk_bf16_f32 v20, v28, s0
	v_mul_f32_e32 v26, v85, v30
	global_store_short v[22:23], v19, off offset:-4096
	global_store_short v[24:25], v20, off offset:2048
	v_cvt_pk_bf16_f32 v19, v21, s0
	v_cvt_pk_bf16_f32 v18, v18, s0
	v_cvt_pk_bf16_f32 v20, v26, s0
	global_store_short v[22:23], v19, off
	global_store_short v[22:23], v20, off offset:2048
	global_store_short v[16:17], v18, off
	s_cbranch_scc0 .LBB0_807
	s_add_i32 s54, s54, s55
	s_add_i32 s58, s58, s59
	s_cmpk_gt_i32 s54, 0xff
	s_cbranch_scc0 .LBB0_739
	v_readlane_b32 s60, v255, 11
